# v15 = v13 + norm3 context-row partial-sum block hand-written: 24 loads in flight instead of near-serial round trips (same add order)
# speedup vs baseline: 1.0012x; 1.0012x over previous
;     ...
;         const float4* x = (const float4*)(row < NL ? src_lat + (size_t)row * DM : src_ctx + (size_t)(row - NL) * DM);
;         float4 v[8];
; #pragma unroll
;         for (int q = 0; q < 8; ++q) v[q] = x[lane + 64 * q];
;         if (part != nullptr && row >= NL) {
; #pragma unroll
;             for (int q = 0; q < 8; ++q) {
;                 float4 a = make_float4(0.f, 0.f, 0.f, 0.f);
;                 for (int sidx = 0; sidx < nparts; ++sidx) { const float4 t = ((const float4*)(part + ((size_t)sidx * NC + (row - NL)) * DM))[lane + 64 * q]; a.x += t.x; a.y += t.y; a.z += t.z; a.w += t.w; }
;                 const float4 g4 = ((const float4*)pgate)[lane + 64 * q];
;                 v[q].x += g4.x * a.x; v[q].y += g4.y * a.y; v[q].z += g4.z * a.z; v[q].w += g4.w * a.w;
.LBB0_1280:
	v_readlane_b32 s36, v248, 9
	s_movk_i32 s0, 0x2000
	v_readlane_b32 s41, v248, 14
	v_add_u32_e32 v76, 0xffffe000, v104
	v_cmp_gt_i32_e64 s[0:1], s0, v104
	v_mov_b32_e32 v4, s13
	v_readlane_b32 s40, v248, 13
	v_mov_b32_e32 v5, s41
	v_cndmask_b32_e64 v3, 0, v105, s[0:1]
	v_cndmask_b32_e64 v2, v76, v104, s[0:1]
	v_cndmask_b32_e64 v5, v4, v5, s[0:1]
	v_mov_b32_e32 v4, s12
	v_mov_b32_e32 v6, s40
	v_cndmask_b32_e64 v4, v4, v6, s[0:1]
	v_lshlrev_b64 v[2:3], 13, v[2:3]
	v_lshl_add_u64 v[2:3], v[4:5], 0, v[2:3]
	v_lshlrev_b32_e32 v122, 4, v74
	v_mov_b32_e32 v123, v77
	v_lshl_add_u64 v[4:5], v[2:3], 0, v[122:123]
	v_mov_b32_e32 v109, v77
	global_load_dwordx4 v[30:33], v[4:5], off
	global_load_dwordx4 v[26:29], v[4:5], off offset:1024
	global_load_dwordx4 v[22:25], v[4:5], off offset:2048
	global_load_dwordx4 v[18:21], v[4:5], off offset:3072
	v_lshl_add_u64 v[4:5], v[2:3], 0, v[108:109]
	v_mov_b32_e32 v111, v77
	v_mov_b32_e32 v113, v77
	v_mov_b32_e32 v115, v77
	v_lshl_add_u64 v[6:7], v[2:3], 0, v[110:111]
	global_load_dwordx4 v[14:17], v[4:5], off
	global_load_dwordx4 v[10:13], v[6:7], off
	v_lshl_add_u64 v[4:5], v[2:3], 0, v[112:113]
	v_lshl_add_u64 v[2:3], v[2:3], 0, v[114:115]
	global_load_dwordx4 v[6:9], v[4:5], off
	s_nop 0
	global_load_dwordx4 v[2:5], v[2:3], off
	s_movk_i32 s16, 0x1fff
	v_cmp_lt_i32_e32 vcc, s16, v104
	s_and_b64 s[24:25], s[8:9], vcc
	v_readlane_b32 s37, v248, 10
	v_readlane_b32 s38, v248, 11
	v_readlane_b32 s39, v248, 12
	v_readlane_b32 s42, v248, 15
	v_readlane_b32 s43, v248, 16
	v_readlane_b32 s44, v248, 17
	v_readlane_b32 s45, v248, 18
	v_readlane_b32 s46, v248, 19
	v_readlane_b32 s47, v248, 20
	v_readlane_b32 s48, v248, 21
	v_readlane_b32 s49, v248, 22
	v_readlane_b32 s50, v248, 23
	v_readlane_b32 s51, v248, 24
	s_and_saveexec_b64 s[16:17], s[24:25]
	s_cbranch_execz .LBB0_1279
	v_readlane_b32 s36, v247, 51
	v_readlane_b32 s44, v247, 59
	v_readlane_b32 s45, v247, 60
	v_readlane_b32 s37, v247, 52
	v_readlane_b32 s38, v247, 53
	v_readlane_b32 s39, v247, 54
	v_readlane_b32 s40, v247, 55
	v_readlane_b32 s41, v247, 56
	v_readlane_b32 s42, v247, 57
	v_readlane_b32 s43, v247, 58
	v_readlane_b32 s46, v247, 61
	v_readlane_b32 s47, v247, 62
	v_readlane_b32 s48, v247, 63
	v_readlane_b32 s49, v248, 0
	v_readlane_b32 s50, v248, 1
	v_readlane_b32 s51, v248, 2
	s_nop 1
	v_lshlrev_b64 v[166:167], 13, v[76:77]
	v_lshl_add_u64 v[166:167], s[44:45], 0, v[166:167]
	v_lshl_add_u64 v[166:167], v[166:167], 0, v[122:123]
	v_add_co_u32_e32 v136, vcc, 0x1000, v166
	s_nop 1
	v_addc_co_u32_e32 v137, vcc, 0, v167, vcc
	v_add_co_u32_e32 v138, vcc, 0x401000, v166
	s_nop 1
	v_addc_co_u32_e32 v139, vcc, 0, v167, vcc
	v_add_co_u32_e32 v140, vcc, 0x801000, v166
	s_nop 1
	v_addc_co_u32_e32 v141, vcc, 0, v167, vcc
	v_add_co_u32_e32 v142, vcc, 0xc01000, v166
	s_nop 1
	v_addc_co_u32_e32 v143, vcc, 0, v167, vcc
	v_add_co_u32_e32 v144, vcc, 0x1001000, v166
	s_nop 1
	v_addc_co_u32_e32 v145, vcc, 0, v167, vcc
	v_add_co_u32_e32 v146, vcc, 0x1401000, v166
	s_nop 1
	v_addc_co_u32_e32 v147, vcc, 0, v167, vcc
	v_add_co_u32_e32 v148, vcc, 0x1801000, v166
	s_nop 1
	v_addc_co_u32_e32 v149, vcc, 0, v167, vcc
	v_add_co_u32_e32 v150, vcc, 0x1c01000, v166
	s_nop 1
	v_addc_co_u32_e32 v151, vcc, 0, v167, vcc
	v_add_co_u32_e32 v152, vcc, 0x2001000, v166
	s_nop 1
	v_addc_co_u32_e32 v153, vcc, 0, v167, vcc
	v_add_co_u32_e32 v154, vcc, 0x2401000, v166
	s_nop 1
	v_addc_co_u32_e32 v155, vcc, 0, v167, vcc
	v_add_co_u32_e32 v156, vcc, 0x2801000, v166
	s_nop 1
	v_addc_co_u32_e32 v157, vcc, 0, v167, vcc
	global_load_dwordx4 v[190:193], v[136:137], off offset:-4096
	global_load_dwordx4 v[194:197], v[138:139], off offset:-4096
	global_load_dwordx4 v[198:201], v[140:141], off offset:-4096
	global_load_dwordx4 v[202:205], v[142:143], off offset:-4096
	global_load_dwordx4 v[206:209], v[144:145], off offset:-4096
	global_load_dwordx4 v[210:213], v[146:147], off offset:-4096
	global_load_dwordx4 v[214:217], v[148:149], off offset:-4096
	global_load_dwordx4 v[218:221], v[150:151], off offset:-4096
	global_load_dwordx4 v[222:225], v[152:153], off offset:-4096
	global_load_dwordx4 v[226:229], v[154:155], off offset:-4096
	global_load_dwordx4 v[230:233], v[156:157], off offset:-4096
	global_load_dwordx4 v[234:237], v[80:81], off
	global_load_dwordx4 v[34:37], v[136:137], off offset:-3072
	global_load_dwordx4 v[38:41], v[138:139], off offset:-3072
	global_load_dwordx4 v[42:45], v[140:141], off offset:-3072
	global_load_dwordx4 v[46:49], v[142:143], off offset:-3072
	global_load_dwordx4 v[50:53], v[144:145], off offset:-3072
	global_load_dwordx4 v[54:57], v[146:147], off offset:-3072
	global_load_dwordx4 v[58:61], v[148:149], off offset:-3072
	global_load_dwordx4 v[62:65], v[150:151], off offset:-3072
	global_load_dwordx4 v[66:69], v[152:153], off offset:-3072
	global_load_dwordx4 v[70:73], v[154:155], off offset:-3072
	global_load_dwordx4 v[128:131], v[156:157], off offset:-3072
	global_load_dwordx4 v[132:135], v[82:83], off
	s_waitcnt vmcnt(12)
;     ...
;             for (int q = 0; q < 8; ++q) {
;                 float4 a = make_float4(0.f, 0.f, 0.f, 0.f);
;                 for (int sidx = 0; sidx < nparts; ++sidx) { const float4 t = ((const float4*)(part + ((size_t)sidx * NC + (row - NL)) * DM))[lane + 64 * q]; a.x += t.x; a.y += t.y; a.z += t.z; a.w += t.w; }
;                 const float4 g4 = ((const float4*)pgate)[lane + 64 * q];
;                 v[q].x += g4.x * a.x; v[q].y += g4.y * a.y; v[q].z += g4.z * a.z; v[q].w += g4.w * a.w;
	v_pk_add_f32 v[158:159], v[190:191], 0 op_sel_hi:[1,0]
	v_pk_add_f32 v[160:161], v[192:193], 0 op_sel_hi:[1,0]
	v_pk_add_f32 v[158:159], v[158:159], v[194:195]
	v_pk_add_f32 v[160:161], v[160:161], v[196:197]
	v_pk_add_f32 v[158:159], v[158:159], v[198:199]
	v_pk_add_f32 v[160:161], v[160:161], v[200:201]
	v_pk_add_f32 v[158:159], v[158:159], v[202:203]
	v_pk_add_f32 v[160:161], v[160:161], v[204:205]
	v_pk_add_f32 v[158:159], v[158:159], v[206:207]
	v_pk_add_f32 v[160:161], v[160:161], v[208:209]
	v_pk_add_f32 v[158:159], v[158:159], v[210:211]
	v_pk_add_f32 v[160:161], v[160:161], v[212:213]
	v_pk_add_f32 v[158:159], v[158:159], v[214:215]
	v_pk_add_f32 v[160:161], v[160:161], v[216:217]
	v_pk_add_f32 v[158:159], v[158:159], v[218:219]
	v_pk_add_f32 v[160:161], v[160:161], v[220:221]
	v_pk_add_f32 v[158:159], v[158:159], v[222:223]
	v_pk_add_f32 v[160:161], v[160:161], v[224:225]
	v_pk_add_f32 v[158:159], v[158:159], v[226:227]
	v_pk_add_f32 v[160:161], v[160:161], v[228:229]
	v_pk_add_f32 v[158:159], v[158:159], v[230:231]
	v_pk_add_f32 v[160:161], v[160:161], v[232:233]
	v_pk_fma_f32 v[30:31], v[158:159], v[234:235], v[30:31]
	v_pk_fma_f32 v[32:33], v[160:161], v[236:237], v[32:33]
	global_load_dwordx4 v[190:193], v[136:137], off offset:-2048
	global_load_dwordx4 v[194:197], v[138:139], off offset:-2048
	global_load_dwordx4 v[198:201], v[140:141], off offset:-2048
	global_load_dwordx4 v[202:205], v[142:143], off offset:-2048
	global_load_dwordx4 v[206:209], v[144:145], off offset:-2048
	global_load_dwordx4 v[210:213], v[146:147], off offset:-2048
	global_load_dwordx4 v[214:217], v[148:149], off offset:-2048
	global_load_dwordx4 v[218:221], v[150:151], off offset:-2048
	global_load_dwordx4 v[222:225], v[152:153], off offset:-2048
	global_load_dwordx4 v[226:229], v[154:155], off offset:-2048
	global_load_dwordx4 v[230:233], v[156:157], off offset:-2048
	global_load_dwordx4 v[234:237], v[84:85], off
	s_waitcnt vmcnt(12)
	v_pk_add_f32 v[158:159], v[34:35], 0 op_sel_hi:[1,0]
	v_pk_add_f32 v[160:161], v[36:37], 0 op_sel_hi:[1,0]
	v_pk_add_f32 v[158:159], v[158:159], v[38:39]
	v_pk_add_f32 v[160:161], v[160:161], v[40:41]
	v_pk_add_f32 v[158:159], v[158:159], v[42:43]
	v_pk_add_f32 v[160:161], v[160:161], v[44:45]
	v_pk_add_f32 v[158:159], v[158:159], v[46:47]
	v_pk_add_f32 v[160:161], v[160:161], v[48:49]
	v_pk_add_f32 v[158:159], v[158:159], v[50:51]
	v_pk_add_f32 v[160:161], v[160:161], v[52:53]
	v_pk_add_f32 v[158:159], v[158:159], v[54:55]
	v_pk_add_f32 v[160:161], v[160:161], v[56:57]
	v_pk_add_f32 v[158:159], v[158:159], v[58:59]
	v_pk_add_f32 v[160:161], v[160:161], v[60:61]
	v_pk_add_f32 v[158:159], v[158:159], v[62:63]
	v_pk_add_f32 v[160:161], v[160:161], v[64:65]
	v_pk_add_f32 v[158:159], v[158:159], v[66:67]
	v_pk_add_f32 v[160:161], v[160:161], v[68:69]
	v_pk_add_f32 v[158:159], v[158:159], v[70:71]
	v_pk_add_f32 v[160:161], v[160:161], v[72:73]
	v_pk_add_f32 v[158:159], v[158:159], v[128:129]
	v_pk_add_f32 v[160:161], v[160:161], v[130:131]
	v_pk_fma_f32 v[26:27], v[158:159], v[132:133], v[26:27]
	v_pk_fma_f32 v[28:29], v[160:161], v[134:135], v[28:29]
	global_load_dwordx4 v[34:37], v[136:137], off offset:-1024
	global_load_dwordx4 v[38:41], v[138:139], off offset:-1024
	global_load_dwordx4 v[42:45], v[140:141], off offset:-1024
	global_load_dwordx4 v[46:49], v[142:143], off offset:-1024
	global_load_dwordx4 v[50:53], v[144:145], off offset:-1024
	global_load_dwordx4 v[54:57], v[146:147], off offset:-1024
	global_load_dwordx4 v[58:61], v[148:149], off offset:-1024
	global_load_dwordx4 v[62:65], v[150:151], off offset:-1024
	global_load_dwordx4 v[66:69], v[152:153], off offset:-1024
	global_load_dwordx4 v[70:73], v[154:155], off offset:-1024
	global_load_dwordx4 v[128:131], v[156:157], off offset:-1024
	global_load_dwordx4 v[132:135], v[86:87], off
	s_waitcnt vmcnt(12)
	v_pk_add_f32 v[158:159], v[190:191], 0 op_sel_hi:[1,0]
	v_pk_add_f32 v[160:161], v[192:193], 0 op_sel_hi:[1,0]
	v_pk_add_f32 v[158:159], v[158:159], v[194:195]
	v_pk_add_f32 v[160:161], v[160:161], v[196:197]
	v_pk_add_f32 v[158:159], v[158:159], v[198:199]
	v_pk_add_f32 v[160:161], v[160:161], v[200:201]
	v_pk_add_f32 v[158:159], v[158:159], v[202:203]
	v_pk_add_f32 v[160:161], v[160:161], v[204:205]
	v_pk_add_f32 v[158:159], v[158:159], v[206:207]
	v_pk_add_f32 v[160:161], v[160:161], v[208:209]
	v_pk_add_f32 v[158:159], v[158:159], v[210:211]
	v_pk_add_f32 v[160:161], v[160:161], v[212:213]
	v_pk_add_f32 v[158:159], v[158:159], v[214:215]
	v_pk_add_f32 v[160:161], v[160:161], v[216:217]
	v_pk_add_f32 v[158:159], v[158:159], v[218:219]
	v_pk_add_f32 v[160:161], v[160:161], v[220:221]
	v_pk_add_f32 v[158:159], v[158:159], v[222:223]
	v_pk_add_f32 v[160:161], v[160:161], v[224:225]
	v_pk_add_f32 v[158:159], v[158:159], v[226:227]
	v_pk_add_f32 v[160:161], v[160:161], v[228:229]
	v_pk_add_f32 v[158:159], v[158:159], v[230:231]
	v_pk_add_f32 v[160:161], v[160:161], v[232:233]
	v_pk_fma_f32 v[22:23], v[158:159], v[234:235], v[22:23]
	v_pk_fma_f32 v[24:25], v[160:161], v[236:237], v[24:25]
	global_load_dwordx4 v[190:193], v[136:137], off
	global_load_dwordx4 v[194:197], v[138:139], off
	global_load_dwordx4 v[198:201], v[140:141], off
	global_load_dwordx4 v[202:205], v[142:143], off
	global_load_dwordx4 v[206:209], v[144:145], off
	global_load_dwordx4 v[210:213], v[146:147], off
	global_load_dwordx4 v[214:217], v[148:149], off
	global_load_dwordx4 v[218:221], v[150:151], off
	global_load_dwordx4 v[222:225], v[152:153], off
	global_load_dwordx4 v[226:229], v[154:155], off
	global_load_dwordx4 v[230:233], v[156:157], off
	global_load_dwordx4 v[234:237], v[88:89], off
	s_waitcnt vmcnt(12)
;     ...
;             for (int q = 0; q < 8; ++q) {
;                 float4 a = make_float4(0.f, 0.f, 0.f, 0.f);
;                 for (int sidx = 0; sidx < nparts; ++sidx) { const float4 t = ((const float4*)(part + ((size_t)sidx * NC + (row - NL)) * DM))[lane + 64 * q]; a.x += t.x; a.y += t.y; a.z += t.z; a.w += t.w; }
;                 const float4 g4 = ((const float4*)pgate)[lane + 64 * q];
;                 v[q].x += g4.x * a.x; v[q].y += g4.y * a.y; v[q].z += g4.z * a.z; v[q].w += g4.w * a.w;
	v_pk_add_f32 v[158:159], v[34:35], 0 op_sel_hi:[1,0]
	v_pk_add_f32 v[160:161], v[36:37], 0 op_sel_hi:[1,0]
	v_pk_add_f32 v[158:159], v[158:159], v[38:39]
	v_pk_add_f32 v[160:161], v[160:161], v[40:41]
	v_pk_add_f32 v[158:159], v[158:159], v[42:43]
	v_pk_add_f32 v[160:161], v[160:161], v[44:45]
	v_pk_add_f32 v[158:159], v[158:159], v[46:47]
	v_pk_add_f32 v[160:161], v[160:161], v[48:49]
	v_pk_add_f32 v[158:159], v[158:159], v[50:51]
	v_pk_add_f32 v[160:161], v[160:161], v[52:53]
	v_pk_add_f32 v[158:159], v[158:159], v[54:55]
	v_pk_add_f32 v[160:161], v[160:161], v[56:57]
	v_pk_add_f32 v[158:159], v[158:159], v[58:59]
	v_pk_add_f32 v[160:161], v[160:161], v[60:61]
	v_pk_add_f32 v[158:159], v[158:159], v[62:63]
	v_pk_add_f32 v[160:161], v[160:161], v[64:65]
	v_pk_add_f32 v[158:159], v[158:159], v[66:67]
	v_pk_add_f32 v[160:161], v[160:161], v[68:69]
	v_pk_add_f32 v[158:159], v[158:159], v[70:71]
	v_pk_add_f32 v[160:161], v[160:161], v[72:73]
	v_pk_add_f32 v[158:159], v[158:159], v[128:129]
	v_pk_add_f32 v[160:161], v[160:161], v[130:131]
	v_pk_fma_f32 v[18:19], v[158:159], v[132:133], v[18:19]
	v_pk_fma_f32 v[20:21], v[160:161], v[134:135], v[20:21]
	global_load_dwordx4 v[34:37], v[136:137], off offset:1024
	global_load_dwordx4 v[38:41], v[138:139], off offset:1024
	global_load_dwordx4 v[42:45], v[140:141], off offset:1024
	global_load_dwordx4 v[46:49], v[142:143], off offset:1024
	global_load_dwordx4 v[50:53], v[144:145], off offset:1024
	global_load_dwordx4 v[54:57], v[146:147], off offset:1024
	global_load_dwordx4 v[58:61], v[148:149], off offset:1024
	global_load_dwordx4 v[62:65], v[150:151], off offset:1024
	global_load_dwordx4 v[66:69], v[152:153], off offset:1024
	global_load_dwordx4 v[70:73], v[154:155], off offset:1024
	global_load_dwordx4 v[128:131], v[156:157], off offset:1024
	global_load_dwordx4 v[132:135], v[90:91], off
	s_waitcnt vmcnt(12)
	v_pk_add_f32 v[158:159], v[190:191], 0 op_sel_hi:[1,0]
	v_pk_add_f32 v[160:161], v[192:193], 0 op_sel_hi:[1,0]
	v_pk_add_f32 v[158:159], v[158:159], v[194:195]
	v_pk_add_f32 v[160:161], v[160:161], v[196:197]
	v_pk_add_f32 v[158:159], v[158:159], v[198:199]
	v_pk_add_f32 v[160:161], v[160:161], v[200:201]
	v_pk_add_f32 v[158:159], v[158:159], v[202:203]
	v_pk_add_f32 v[160:161], v[160:161], v[204:205]
	v_pk_add_f32 v[158:159], v[158:159], v[206:207]
	v_pk_add_f32 v[160:161], v[160:161], v[208:209]
	v_pk_add_f32 v[158:159], v[158:159], v[210:211]
	v_pk_add_f32 v[160:161], v[160:161], v[212:213]
	v_pk_add_f32 v[158:159], v[158:159], v[214:215]
	v_pk_add_f32 v[160:161], v[160:161], v[216:217]
	v_pk_add_f32 v[158:159], v[158:159], v[218:219]
	v_pk_add_f32 v[160:161], v[160:161], v[220:221]
	v_pk_add_f32 v[158:159], v[158:159], v[222:223]
	v_pk_add_f32 v[160:161], v[160:161], v[224:225]
	v_pk_add_f32 v[158:159], v[158:159], v[226:227]
	v_pk_add_f32 v[160:161], v[160:161], v[228:229]
	v_pk_add_f32 v[158:159], v[158:159], v[230:231]
	v_pk_add_f32 v[160:161], v[160:161], v[232:233]
	v_pk_fma_f32 v[14:15], v[158:159], v[234:235], v[14:15]
	v_pk_fma_f32 v[16:17], v[160:161], v[236:237], v[16:17]
	global_load_dwordx4 v[190:193], v[136:137], off offset:2048
	global_load_dwordx4 v[194:197], v[138:139], off offset:2048
	global_load_dwordx4 v[198:201], v[140:141], off offset:2048
	global_load_dwordx4 v[202:205], v[142:143], off offset:2048
	global_load_dwordx4 v[206:209], v[144:145], off offset:2048
	global_load_dwordx4 v[210:213], v[146:147], off offset:2048
	global_load_dwordx4 v[214:217], v[148:149], off offset:2048
	global_load_dwordx4 v[218:221], v[150:151], off offset:2048
	global_load_dwordx4 v[222:225], v[152:153], off offset:2048
	global_load_dwordx4 v[226:229], v[154:155], off offset:2048
	global_load_dwordx4 v[230:233], v[156:157], off offset:2048
	global_load_dwordx4 v[234:237], v[92:93], off
	s_waitcnt vmcnt(12)
;     ...
;             for (int q = 0; q < 8; ++q) {
;                 float4 a = make_float4(0.f, 0.f, 0.f, 0.f);
;                 for (int sidx = 0; sidx < nparts; ++sidx) { const float4 t = ((const float4*)(part + ((size_t)sidx * NC + (row - NL)) * DM))[lane + 64 * q]; a.x += t.x; a.y += t.y; a.z += t.z; a.w += t.w; }
;                 const float4 g4 = ((const float4*)pgate)[lane + 64 * q];
;                 v[q].x += g4.x * a.x; v[q].y += g4.y * a.y; v[q].z += g4.z * a.z; v[q].w += g4.w * a.w;
	v_pk_add_f32 v[158:159], v[34:35], 0 op_sel_hi:[1,0]
	v_pk_add_f32 v[160:161], v[36:37], 0 op_sel_hi:[1,0]
	v_pk_add_f32 v[158:159], v[158:159], v[38:39]
	v_pk_add_f32 v[160:161], v[160:161], v[40:41]
	v_pk_add_f32 v[158:159], v[158:159], v[42:43]
	v_pk_add_f32 v[160:161], v[160:161], v[44:45]
	v_pk_add_f32 v[158:159], v[158:159], v[46:47]
	v_pk_add_f32 v[160:161], v[160:161], v[48:49]
	v_pk_add_f32 v[158:159], v[158:159], v[50:51]
	v_pk_add_f32 v[160:161], v[160:161], v[52:53]
	v_pk_add_f32 v[158:159], v[158:159], v[54:55]
	v_pk_add_f32 v[160:161], v[160:161], v[56:57]
	v_pk_add_f32 v[158:159], v[158:159], v[58:59]
	v_pk_add_f32 v[160:161], v[160:161], v[60:61]
	v_pk_add_f32 v[158:159], v[158:159], v[62:63]
	v_pk_add_f32 v[160:161], v[160:161], v[64:65]
	v_pk_add_f32 v[158:159], v[158:159], v[66:67]
	v_pk_add_f32 v[160:161], v[160:161], v[68:69]
	v_pk_add_f32 v[158:159], v[158:159], v[70:71]
	v_pk_add_f32 v[160:161], v[160:161], v[72:73]
	v_pk_add_f32 v[158:159], v[158:159], v[128:129]
	v_pk_add_f32 v[160:161], v[160:161], v[130:131]
	v_pk_fma_f32 v[10:11], v[158:159], v[132:133], v[10:11]
	v_pk_fma_f32 v[12:13], v[160:161], v[134:135], v[12:13]
	global_load_dwordx4 v[34:37], v[136:137], off offset:3072
	global_load_dwordx4 v[38:41], v[138:139], off offset:3072
	global_load_dwordx4 v[42:45], v[140:141], off offset:3072
	global_load_dwordx4 v[46:49], v[142:143], off offset:3072
	global_load_dwordx4 v[50:53], v[144:145], off offset:3072
	global_load_dwordx4 v[54:57], v[146:147], off offset:3072
	global_load_dwordx4 v[58:61], v[148:149], off offset:3072
	global_load_dwordx4 v[62:65], v[150:151], off offset:3072
	global_load_dwordx4 v[66:69], v[152:153], off offset:3072
	global_load_dwordx4 v[70:73], v[154:155], off offset:3072
	global_load_dwordx4 v[128:131], v[156:157], off offset:3072
	global_load_dwordx4 v[132:135], v[94:95], off
	s_waitcnt vmcnt(12)
	v_pk_add_f32 v[158:159], v[190:191], 0 op_sel_hi:[1,0]
	v_pk_add_f32 v[160:161], v[192:193], 0 op_sel_hi:[1,0]
	v_pk_add_f32 v[158:159], v[158:159], v[194:195]
	v_pk_add_f32 v[160:161], v[160:161], v[196:197]
	v_pk_add_f32 v[158:159], v[158:159], v[198:199]
	v_pk_add_f32 v[160:161], v[160:161], v[200:201]
	v_pk_add_f32 v[158:159], v[158:159], v[202:203]
	v_pk_add_f32 v[160:161], v[160:161], v[204:205]
	v_pk_add_f32 v[158:159], v[158:159], v[206:207]
	v_pk_add_f32 v[160:161], v[160:161], v[208:209]
	v_pk_add_f32 v[158:159], v[158:159], v[210:211]
	v_pk_add_f32 v[160:161], v[160:161], v[212:213]
	v_pk_add_f32 v[158:159], v[158:159], v[214:215]
	v_pk_add_f32 v[160:161], v[160:161], v[216:217]
	v_pk_add_f32 v[158:159], v[158:159], v[218:219]
	v_pk_add_f32 v[160:161], v[160:161], v[220:221]
	v_pk_add_f32 v[158:159], v[158:159], v[222:223]
	v_pk_add_f32 v[160:161], v[160:161], v[224:225]
	v_pk_add_f32 v[158:159], v[158:159], v[226:227]
	v_pk_add_f32 v[160:161], v[160:161], v[228:229]
	v_pk_add_f32 v[158:159], v[158:159], v[230:231]
	v_pk_add_f32 v[160:161], v[160:161], v[232:233]
	v_pk_fma_f32 v[6:7], v[158:159], v[234:235], v[6:7]
	v_pk_fma_f32 v[8:9], v[160:161], v[236:237], v[8:9]
	s_waitcnt vmcnt(0)
	v_pk_add_f32 v[158:159], v[34:35], 0 op_sel_hi:[1,0]
	v_pk_add_f32 v[160:161], v[36:37], 0 op_sel_hi:[1,0]
	v_pk_add_f32 v[158:159], v[158:159], v[38:39]
	v_pk_add_f32 v[160:161], v[160:161], v[40:41]
	v_pk_add_f32 v[158:159], v[158:159], v[42:43]
	v_pk_add_f32 v[160:161], v[160:161], v[44:45]
	v_pk_add_f32 v[158:159], v[158:159], v[46:47]
	v_pk_add_f32 v[160:161], v[160:161], v[48:49]
	v_pk_add_f32 v[158:159], v[158:159], v[50:51]
	v_pk_add_f32 v[160:161], v[160:161], v[52:53]
	v_pk_add_f32 v[158:159], v[158:159], v[54:55]
	v_pk_add_f32 v[160:161], v[160:161], v[56:57]
	v_pk_add_f32 v[158:159], v[158:159], v[58:59]
	v_pk_add_f32 v[160:161], v[160:161], v[60:61]
	v_pk_add_f32 v[158:159], v[158:159], v[62:63]
	v_pk_add_f32 v[160:161], v[160:161], v[64:65]
	v_pk_add_f32 v[158:159], v[158:159], v[66:67]
	v_pk_add_f32 v[160:161], v[160:161], v[68:69]
	v_pk_add_f32 v[158:159], v[158:159], v[70:71]
	v_pk_add_f32 v[160:161], v[160:161], v[72:73]
	v_pk_add_f32 v[158:159], v[158:159], v[128:129]
	v_pk_add_f32 v[160:161], v[160:161], v[130:131]
	v_pk_fma_f32 v[2:3], v[158:159], v[132:133], v[2:3]
	v_pk_fma_f32 v[4:5], v[160:161], v[134:135], v[4:5]
	s_branch .LBB0_1279
